# speedup vs baseline: 1.0179x; 1.0103x over previous
.LBB0_8:
	s_load_dwordx4 s[4:7], s[0:1], 0x0
	v_and_b32_e32 v1, 63, v0
	s_cmpk_gt_i32 s12, 0xff
	s_mov_b64 s[2:3], -1
	s_cbranch_scc0 .LBB0_24
	v_and_b32_e32 v74, 31, v0
	v_lshrrev_b32_e32 v75, 5, v1
	v_lshrrev_b32_e32 v76, 6, v0
	s_lshl_b32 s8, s12, 2
	s_cmpk_gt_u32 s12, 0x1ff
	v_mov_b32_e32 v39, 0
	v_add_u32_e32 v77, s8, v76
	v_lshlrev_b32_e32 v36, 2, v74
	v_lshlrev_b32_e32 v34, 17, v75
	s_cbranch_scc0 .LBB0_11
	v_add_u32_e32 v4, 0xfffff800, v77
	s_load_dwordx2 s[2:3], s[0:1], 0x30
	v_lshrrev_b32_e32 v2, 2, v4
	v_and_b32_e32 v38, 0x3fffffc0, v2
	v_lshlrev_b64 v[2:3], 14, v[38:39]
	v_lshlrev_b32_e32 v4, 6, v4
	v_bfe_u32 v78, v0, 6, 1
	s_waitcnt lgkmcnt(0)
	v_lshl_add_u64 v[2:3], s[6:7], 0, v[2:3]
	v_and_b32_e32 v40, 0x3f80, v4
	v_mov_b32_e32 v41, v39
	v_lshlrev_b32_e32 v4, 8, v74
	v_lshl_add_u64 v[2:3], v[2:3], 0, v[40:41]
	v_mov_b32_e32 v37, v39
	v_lshl_or_b32 v4, v78, 13, v4
	v_mov_b32_e32 v5, v39
	v_lshl_add_u64 v[2:3], v[2:3], 0, v[36:37]
	v_lshl_add_u64 v[4:5], s[2:3], 0, v[4:5]
	v_lshlrev_b32_e32 v6, 5, v75
	v_mov_b32_e32 v7, v39
	v_mov_b32_e32 v35, v39
	v_lshl_add_u64 v[42:43], v[4:5], 0, v[6:7]
	v_lshl_add_u64 v[44:45], v[2:3], 0, v[34:35]
	s_movk_i32 s2, 0x4000
	global_load_dwordx4 v[26:29], v[42:43], off offset:16
	global_load_dwordx4 v[30:33], v[42:43], off
	global_load_dwordx4 v[18:21], v[42:43], off offset:80
	global_load_dwordx4 v[22:25], v[42:43], off offset:64
	global_load_dwordx4 v[10:13], v[42:43], off offset:144
	global_load_dwordx4 v[14:17], v[42:43], off offset:128
	global_load_dwordx4 v[2:5], v[42:43], off offset:208
	global_load_dwordx4 v[6:9], v[42:43], off offset:192
	v_add_co_u32_e32 v42, vcc, s2, v44
	s_mov_b32 s3, 0x8000
	s_nop 0
	v_addc_co_u32_e32 v43, vcc, 0, v45, vcc
	v_add_co_u32_e32 v46, vcc, s3, v44
	s_mov_b32 s8, 0xc000
	s_nop 0
	v_addc_co_u32_e32 v47, vcc, 0, v45, vcc
	v_add_co_u32_e32 v48, vcc, s8, v44
	s_mov_b32 s9, 0x10000
	s_nop 0
	v_addc_co_u32_e32 v49, vcc, 0, v45, vcc
	v_add_co_u32_e32 v50, vcc, s9, v44
	s_mov_b32 s9, 0x14000
	s_nop 0
	v_addc_co_u32_e32 v51, vcc, 0, v45, vcc
	v_add_co_u32_e32 v52, vcc, s9, v44
	s_mov_b32 s9, 0x18000
	s_nop 0
	v_addc_co_u32_e32 v53, vcc, 0, v45, vcc
	v_add_co_u32_e32 v54, vcc, s9, v44
	s_mov_b32 s9, 0x1c000
	s_nop 0
	v_addc_co_u32_e32 v55, vcc, 0, v45, vcc
	v_add_co_u32_e32 v56, vcc, s9, v44
	s_mov_b32 s9, 0x40000
	s_nop 0
	v_addc_co_u32_e32 v57, vcc, 0, v45, vcc
	global_load_dword v72, v[44:45], off
	global_load_dword v73, v[42:43], off
	global_load_dword v70, v[46:47], off
	global_load_dword v71, v[48:49], off
	global_load_dword v68, v[50:51], off
	global_load_dword v69, v[52:53], off
	global_load_dword v66, v[54:55], off
	global_load_dword v67, v[56:57], off
	v_add_co_u32_e32 v42, vcc, s9, v44
	s_mov_b32 s10, 0x44000
	s_nop 0
	v_addc_co_u32_e32 v43, vcc, 0, v45, vcc
	v_add_co_u32_e32 v46, vcc, s10, v44
	s_mov_b32 s11, 0x48000
	s_nop 0
	v_addc_co_u32_e32 v47, vcc, 0, v45, vcc
	v_add_co_u32_e32 v48, vcc, s11, v44
	s_mov_b32 s13, 0x4c000
	s_nop 0
	v_addc_co_u32_e32 v49, vcc, 0, v45, vcc
	v_add_co_u32_e32 v50, vcc, s13, v44
	s_mov_b32 s14, 0x50000
	s_nop 0
	v_addc_co_u32_e32 v51, vcc, 0, v45, vcc
	v_add_co_u32_e32 v52, vcc, s14, v44
	s_mov_b32 s14, 0x54000
	s_nop 0
	v_addc_co_u32_e32 v53, vcc, 0, v45, vcc
	v_add_co_u32_e32 v54, vcc, s14, v44
	s_mov_b32 s14, 0x58000
	s_nop 0
	v_addc_co_u32_e32 v55, vcc, 0, v45, vcc
	v_add_co_u32_e32 v56, vcc, s14, v44
	s_mov_b32 s14, 0x5c000
	s_nop 0
	v_addc_co_u32_e32 v57, vcc, 0, v45, vcc
	v_add_co_u32_e32 v80, vcc, s14, v44
	s_mov_b32 s14, 0x80000
	s_nop 0
	v_addc_co_u32_e32 v81, vcc, 0, v45, vcc
	global_load_dword v64, v[42:43], off
	global_load_dword v65, v[46:47], off
	global_load_dword v62, v[48:49], off
	global_load_dword v63, v[50:51], off
	global_load_dword v60, v[52:53], off
	global_load_dword v61, v[54:55], off
	global_load_dword v58, v[56:57], off
	global_load_dword v59, v[80:81], off
	v_add_co_u32_e32 v42, vcc, s14, v44
	s_mov_b32 s14, 0x84000
	s_nop 0
	v_addc_co_u32_e32 v43, vcc, 0, v45, vcc
	v_add_co_u32_e32 v46, vcc, s14, v44
	s_mov_b32 s14, 0x88000
	s_nop 0
	v_addc_co_u32_e32 v47, vcc, 0, v45, vcc
	v_add_co_u32_e32 v48, vcc, s14, v44
	s_mov_b32 s14, 0x8c000
	s_nop 0
	v_addc_co_u32_e32 v49, vcc, 0, v45, vcc
	v_add_co_u32_e32 v54, vcc, s14, v44
	s_mov_b32 s14, 0x90000
	s_nop 0
	v_addc_co_u32_e32 v55, vcc, 0, v45, vcc
	v_add_co_u32_e32 v80, vcc, s14, v44
	s_mov_b32 s14, 0x94000
	s_nop 0
	v_addc_co_u32_e32 v81, vcc, 0, v45, vcc
	v_add_co_u32_e32 v82, vcc, s14, v44
	s_mov_b32 s14, 0x98000
	s_nop 0
	v_addc_co_u32_e32 v83, vcc, 0, v45, vcc
	global_load_dword v56, v[42:43], off
	global_load_dword v57, v[46:47], off
	global_load_dword v52, v[48:49], off
	global_load_dword v53, v[54:55], off
	global_load_dword v50, v[80:81], off
	global_load_dword v51, v[82:83], off
	v_add_co_u32_e32 v42, vcc, s14, v44
	s_mov_b32 s14, 0x9c000
	s_nop 0
	v_addc_co_u32_e32 v43, vcc, 0, v45, vcc
	v_add_co_u32_e32 v46, vcc, s14, v44
	s_mov_b32 s14, 0xc0000
	s_nop 0
	v_addc_co_u32_e32 v47, vcc, 0, v45, vcc
	global_load_dword v54, v[42:43], off
	global_load_dword v55, v[46:47], off
	v_add_co_u32_e32 v80, vcc, s14, v44
	s_mov_b32 s14, 0xc4000
	s_nop 0
	v_addc_co_u32_e32 v81, vcc, 0, v45, vcc
	v_add_co_u32_e32 v82, vcc, s14, v44
	s_mov_b32 s14, 0xc8000
	s_nop 0
	v_addc_co_u32_e32 v83, vcc, 0, v45, vcc
	v_add_co_u32_e32 v84, vcc, s14, v44
	s_mov_b32 s14, 0xcc000
	s_nop 0
	v_addc_co_u32_e32 v85, vcc, 0, v45, vcc
	v_add_co_u32_e32 v86, vcc, s14, v44
	s_mov_b32 s14, 0xd0000
	s_nop 0
	v_addc_co_u32_e32 v87, vcc, 0, v45, vcc
	v_add_co_u32_e32 v88, vcc, s14, v44
	s_mov_b32 s14, 0xd4000
	s_nop 0
	v_addc_co_u32_e32 v89, vcc, 0, v45, vcc
	v_add_co_u32_e32 v90, vcc, s14, v44
	s_mov_b32 s14, 0xd8000
	s_nop 0
	v_addc_co_u32_e32 v91, vcc, 0, v45, vcc
	v_add_co_u32_e32 v92, vcc, s14, v44
	s_mov_b32 s14, 0xdc000
	s_nop 0
	v_addc_co_u32_e32 v93, vcc, 0, v45, vcc
	v_add_co_u32_e32 v94, vcc, s14, v44
	s_load_dwordx2 s[14:15], s[0:1], 0x58
	s_nop 0
	v_addc_co_u32_e32 v95, vcc, 0, v45, vcc
	global_load_dword v48, v[80:81], off
	global_load_dword v49, v[82:83], off
	global_load_dword v46, v[84:85], off
	global_load_dword v47, v[86:87], off
	global_load_dword v44, v[88:89], off
	global_load_dword v45, v[90:91], off
	global_load_dword v42, v[92:93], off
	global_load_dword v43, v[94:95], off
	s_waitcnt vmcnt(38)
	s_waitcnt vmcnt(31)
	s_waitcnt vmcnt(30)
	s_waitcnt vmcnt(29)
	s_waitcnt vmcnt(28)
	s_waitcnt vmcnt(27)
	s_waitcnt vmcnt(26)
	s_waitcnt vmcnt(25)
	s_waitcnt vmcnt(24)
	s_waitcnt vmcnt(23)
	s_waitcnt vmcnt(22)
	s_waitcnt vmcnt(21)
	s_waitcnt vmcnt(20)
	s_waitcnt vmcnt(19)
	s_waitcnt vmcnt(18)
	s_waitcnt vmcnt(17)
	s_waitcnt vmcnt(16)
	v_cvt_pk_bf16_f32 v35, v72, 0
	v_cvt_pk_bf16_f32 v79, v73, 0
	v_lshlrev_b32_e32 v81, 16, v79
	v_lshlrev_b32_e32 v80, 16, v35
	v_pk_add_f32 v[82:83], v[72:73], v[80:81] neg_lo:[0,1] neg_hi:[0,1]
	v_cvt_pk_bf16_f32 v35, v70, 0
	v_cvt_pk_bf16_f32 v73, v71, 0
	v_lshlrev_b32_e32 v72, 16, v35
	v_lshlrev_b32_e32 v73, 16, v73
	v_pk_add_f32 v[84:85], v[70:71], v[72:73] neg_lo:[0,1] neg_hi:[0,1]
	v_cvt_pk_bf16_f32 v35, v68, 0
	v_cvt_pk_bf16_f32 v70, v69, 0
	v_lshlrev_b32_e32 v86, 16, v35
	v_lshlrev_b32_e32 v87, 16, v70
	v_pk_add_f32 v[88:89], v[68:69], v[86:87] neg_lo:[0,1] neg_hi:[0,1]
	v_cvt_pk_bf16_f32 v35, v66, 0
	v_cvt_pk_bf16_f32 v68, v67, 0
	v_lshlrev_b32_e32 v90, 16, v35
	v_lshlrev_b32_e32 v91, 16, v68
	v_pk_add_f32 v[92:93], v[66:67], v[90:91] neg_lo:[0,1] neg_hi:[0,1]
	v_cvt_pk_bf16_f32 v35, v30, 0
	v_cvt_pk_bf16_f32 v66, v31, 0
	v_cvt_pk_bf16_f32 v68, v26, 0
	v_lshlrev_b32_e32 v67, 16, v66
	v_lshlrev_b32_e32 v66, 16, v35
	v_cvt_pk_bf16_f32 v35, v27, 0
	v_lshlrev_b32_e32 v69, 16, v35
	v_lshlrev_b32_e32 v68, 16, v68
	v_pk_add_f32 v[94:95], v[26:27], v[68:69] neg_lo:[0,1] neg_hi:[0,1]
	v_cvt_pk_bf16_f32 v26, v32, 0
	v_cvt_pk_bf16_f32 v35, v28, 0
	v_cvt_pk_bf16_f32 v27, v33, 0
	v_cvt_pk_bf16_f32 v70, v29, 0
	v_lshlrev_b32_e32 v26, 16, v26
	v_lshlrev_b32_e32 v27, 16, v27
	v_lshlrev_b32_e32 v96, 16, v35
	v_lshlrev_b32_e32 v97, 16, v70
	v_pk_add_f32 v[30:31], v[30:31], v[66:67] neg_lo:[0,1] neg_hi:[0,1]
	v_cvt_pk_bf16_f32 v66, v66, v67
	v_cvt_pk_bf16_f32 v67, v26, v27
	v_cvt_pk_bf16_f32 v68, v68, v69
	v_cvt_pk_bf16_f32 v69, v96, v97
	v_cvt_pk_bf16_f32 v70, v80, v81
	v_cvt_pk_bf16_f32 v71, v72, v73
	v_cvt_pk_bf16_f32 v72, v86, v87
	v_cvt_pk_bf16_f32 v73, v90, v91
	v_pk_add_f32 v[32:33], v[32:33], v[26:27] neg_lo:[0,1] neg_hi:[0,1]
	v_pk_add_f32 v[80:81], v[28:29], v[96:97] neg_lo:[0,1] neg_hi:[0,1]
	v_mfma_f32_32x32x16_bf16 a[0:15], v[66:69], v[70:73], 0
	v_cvt_pk_bf16_f32 v26, v82, v83
	v_cvt_pk_bf16_f32 v27, v84, v85
	v_cvt_pk_bf16_f32 v28, v88, v89
	v_cvt_pk_bf16_f32 v29, v92, v93
	v_cvt_pk_bf16_f32 v30, v30, v31
	v_cvt_pk_bf16_f32 v31, v32, v33
	v_cvt_pk_bf16_f32 v32, v94, v95
	v_mfma_f32_32x32x16_bf16 a[0:15], v[66:69], v[26:29], a[0:15]
	v_cvt_pk_bf16_f32 v33, v80, v81
	v_cvt_pk_bf16_f32 v26, v64, 0
	v_cvt_pk_bf16_f32 v27, v65, 0
	v_cvt_pk_bf16_f32 v28, v18, 0
	v_cvt_pk_bf16_f32 v29, v19, 0
	v_lshlrev_b32_e32 v29, 16, v29
	v_lshlrev_b32_e32 v28, 16, v28
	v_mfma_f32_32x32x16_bf16 a[0:15], v[30:33], v[70:73], a[0:15]
	v_lshlrev_b32_e32 v30, 16, v26
	v_lshlrev_b32_e32 v31, 16, v27
	v_cvt_pk_bf16_f32 v26, v62, 0
	v_cvt_pk_bf16_f32 v27, v63, 0
	v_lshlrev_b32_e32 v32, 16, v26
	v_lshlrev_b32_e32 v33, 16, v27
	v_cvt_pk_bf16_f32 v26, v60, 0
	v_cvt_pk_bf16_f32 v27, v61, 0
	v_lshlrev_b32_e32 v66, 16, v26
	v_lshlrev_b32_e32 v67, 16, v27
	v_cvt_pk_bf16_f32 v26, v58, 0
	v_cvt_pk_bf16_f32 v27, v59, 0
	v_lshlrev_b32_e32 v68, 16, v26
	v_lshlrev_b32_e32 v69, 16, v27
	v_cvt_pk_bf16_f32 v26, v22, 0
	v_cvt_pk_bf16_f32 v27, v23, 0
	v_pk_add_f32 v[70:71], v[18:19], v[28:29] neg_lo:[0,1] neg_hi:[0,1]
	v_cvt_pk_bf16_f32 v18, v24, 0
	v_cvt_pk_bf16_f32 v35, v20, 0
	v_cvt_pk_bf16_f32 v19, v25, 0
	v_cvt_pk_bf16_f32 v73, v21, 0
	v_lshlrev_b32_e32 v27, 16, v27
	v_lshlrev_b32_e32 v26, 16, v26
	v_lshlrev_b32_e32 v18, 16, v18
	v_lshlrev_b32_e32 v19, 16, v19
	v_lshlrev_b32_e32 v72, 16, v35
	v_lshlrev_b32_e32 v73, 16, v73
	v_pk_add_f32 v[22:23], v[22:23], v[26:27] neg_lo:[0,1] neg_hi:[0,1]
	v_cvt_pk_bf16_f32 v26, v26, v27
	v_cvt_pk_bf16_f32 v27, v18, v19
	v_cvt_pk_bf16_f32 v28, v28, v29
	v_cvt_pk_bf16_f32 v29, v72, v73
	v_pk_add_f32 v[64:65], v[64:65], v[30:31] neg_lo:[0,1] neg_hi:[0,1]
	v_pk_add_f32 v[62:63], v[62:63], v[32:33] neg_lo:[0,1] neg_hi:[0,1]
	v_cvt_pk_bf16_f32 v30, v30, v31
	v_cvt_pk_bf16_f32 v31, v32, v33
	v_cvt_pk_bf16_f32 v32, v66, v67
	v_cvt_pk_bf16_f32 v33, v68, v69
	v_pk_add_f32 v[60:61], v[60:61], v[66:67] neg_lo:[0,1] neg_hi:[0,1]
	v_pk_add_f32 v[58:59], v[58:59], v[68:69] neg_lo:[0,1] neg_hi:[0,1]
	v_mfma_f32_32x32x16_bf16 a[0:15], v[26:29], v[30:33], a[0:15]
	v_add_f32_e64 v24, v24, -v18
	v_add_f32_e64 v25, v25, -v19
	v_add_f32_e64 v66, v20, -v72
	v_add_f32_e64 v67, v21, -v73
	v_cvt_pk_bf16_f32 v18, v64, v65
	v_cvt_pk_bf16_f32 v19, v62, v63
	v_cvt_pk_bf16_f32 v20, v60, v61
	v_cvt_pk_bf16_f32 v21, v58, v59
	v_cvt_pk_bf16_f32 v22, v22, v23
	v_cvt_pk_bf16_f32 v23, v24, v25
	v_mfma_f32_32x32x16_bf16 a[0:15], v[26:29], v[18:21], a[0:15]
	v_cvt_pk_bf16_f32 v24, v70, v71
	v_cvt_pk_bf16_f32 v25, v66, v67
	s_waitcnt vmcnt(15)
	s_waitcnt vmcnt(14)
	s_waitcnt vmcnt(13)
	s_waitcnt vmcnt(12)
	s_waitcnt vmcnt(11)
	s_waitcnt vmcnt(10)
	s_waitcnt vmcnt(9)
	s_waitcnt vmcnt(8)
	v_cvt_pk_bf16_f32 v20, v10, 0
	v_cvt_pk_bf16_f32 v18, v56, 0
	v_cvt_pk_bf16_f32 v19, v57, 0
	v_mfma_f32_32x32x16_bf16 a[0:15], v[22:25], v[30:33], a[0:15]
	v_lshlrev_b32_e32 v22, 16, v18
	v_lshlrev_b32_e32 v23, 16, v19
	v_cvt_pk_bf16_f32 v18, v52, 0
	v_cvt_pk_bf16_f32 v19, v53, 0
	v_lshlrev_b32_e32 v24, 16, v18
	v_lshlrev_b32_e32 v25, 16, v19
	v_cvt_pk_bf16_f32 v18, v50, 0
	v_cvt_pk_bf16_f32 v19, v51, 0
	v_lshlrev_b32_e32 v30, 16, v18
	v_lshlrev_b32_e32 v31, 16, v19
	v_cvt_pk_bf16_f32 v18, v54, 0
	v_cvt_pk_bf16_f32 v19, v55, 0
	v_cvt_pk_bf16_f32 v21, v11, 0
	v_pk_add_f32 v[32:33], v[50:51], v[30:31] neg_lo:[0,1] neg_hi:[0,1]
	v_lshlrev_b32_e32 v50, 16, v18
	v_lshlrev_b32_e32 v51, 16, v19
	v_lshlrev_b32_e32 v21, 16, v21
	v_lshlrev_b32_e32 v20, 16, v20
	v_pk_add_f32 v[26:27], v[56:57], v[22:23] neg_lo:[0,1] neg_hi:[0,1]
	v_pk_add_f32 v[28:29], v[52:53], v[24:25] neg_lo:[0,1] neg_hi:[0,1]
	v_pk_add_f32 v[52:53], v[54:55], v[50:51] neg_lo:[0,1] neg_hi:[0,1]
	v_cvt_pk_bf16_f32 v18, v14, 0
	v_cvt_pk_bf16_f32 v19, v15, 0
	v_pk_add_f32 v[54:55], v[10:11], v[20:21] neg_lo:[0,1] neg_hi:[0,1]
	v_cvt_pk_bf16_f32 v10, v16, 0
	v_cvt_pk_bf16_f32 v35, v12, 0
	v_cvt_pk_bf16_f32 v11, v17, 0
	v_cvt_pk_bf16_f32 v57, v13, 0
	v_lshlrev_b32_e32 v19, 16, v19
	v_lshlrev_b32_e32 v18, 16, v18
	v_lshlrev_b32_e32 v10, 16, v10
	v_lshlrev_b32_e32 v11, 16, v11
	v_lshlrev_b32_e32 v56, 16, v35
	v_lshlrev_b32_e32 v57, 16, v57
	v_pk_add_f32 v[14:15], v[14:15], v[18:19] neg_lo:[0,1] neg_hi:[0,1]
	v_cvt_pk_bf16_f32 v18, v18, v19
	v_cvt_pk_bf16_f32 v19, v10, v11
	v_cvt_pk_bf16_f32 v20, v20, v21
	v_cvt_pk_bf16_f32 v21, v56, v57
	v_cvt_pk_bf16_f32 v22, v22, v23
	v_cvt_pk_bf16_f32 v23, v24, v25
	v_cvt_pk_bf16_f32 v24, v30, v31
	v_cvt_pk_bf16_f32 v25, v50, v51
	v_pk_add_f32 v[16:17], v[16:17], v[10:11] neg_lo:[0,1] neg_hi:[0,1]
	v_pk_add_f32 v[30:31], v[12:13], v[56:57] neg_lo:[0,1] neg_hi:[0,1]
	v_mfma_f32_32x32x16_bf16 a[0:15], v[18:21], v[22:25], a[0:15]
	v_cvt_pk_bf16_f32 v10, v26, v27
	v_cvt_pk_bf16_f32 v11, v28, v29
	v_cvt_pk_bf16_f32 v12, v32, v33
	v_cvt_pk_bf16_f32 v13, v52, v53
	v_cvt_pk_bf16_f32 v14, v14, v15
	v_cvt_pk_bf16_f32 v15, v16, v17
	v_cvt_pk_bf16_f32 v16, v54, v55
	v_mfma_f32_32x32x16_bf16 a[0:15], v[18:21], v[10:13], a[0:15]
	v_cvt_pk_bf16_f32 v17, v30, v31
	s_waitcnt vmcnt(7)
	s_waitcnt vmcnt(6)
	s_waitcnt vmcnt(5)
	s_waitcnt vmcnt(4)
	s_waitcnt vmcnt(3)
	s_waitcnt vmcnt(2)
	s_waitcnt vmcnt(1)
	s_waitcnt vmcnt(0)
	v_lshl_or_b32 v38, v78, 5, v38
	v_cvt_pk_bf16_f32 v10, v48, 0
	v_cvt_pk_bf16_f32 v11, v49, 0
	v_mfma_f32_32x32x16_bf16 a[0:15], v[14:17], v[22:25], a[0:15]
	v_lshlrev_b32_e32 v14, 16, v10
	v_lshlrev_b32_e32 v15, 16, v11
	v_cvt_pk_bf16_f32 v10, v46, 0
	v_cvt_pk_bf16_f32 v11, v47, 0
	v_lshlrev_b32_e32 v16, 16, v10
	v_lshlrev_b32_e32 v17, 16, v11
	v_cvt_pk_bf16_f32 v10, v44, 0
	v_cvt_pk_bf16_f32 v11, v45, 0
	v_cvt_pk_bf16_f32 v12, v2, 0
	v_cvt_pk_bf16_f32 v13, v3, 0
	v_lshlrev_b32_e32 v22, 16, v10
	v_lshlrev_b32_e32 v23, 16, v11
	v_cvt_pk_bf16_f32 v10, v42, 0
	v_cvt_pk_bf16_f32 v11, v43, 0
	v_lshlrev_b32_e32 v13, 16, v13
	v_lshlrev_b32_e32 v12, 16, v12
	v_lshlrev_b32_e32 v26, 16, v10
	v_lshlrev_b32_e32 v27, 16, v11
	v_cvt_pk_bf16_f32 v10, v6, 0
	v_cvt_pk_bf16_f32 v11, v7, 0
	v_pk_add_f32 v[30:31], v[2:3], v[12:13] neg_lo:[0,1] neg_hi:[0,1]
	v_cvt_pk_bf16_f32 v2, v8, 0
	v_cvt_pk_bf16_f32 v32, v4, 0
	v_cvt_pk_bf16_f32 v3, v9, 0
	v_cvt_pk_bf16_f32 v33, v5, 0
	v_lshlrev_b32_e32 v11, 16, v11
	v_lshlrev_b32_e32 v10, 16, v10
	v_lshlrev_b32_e32 v2, 16, v2
	v_lshlrev_b32_e32 v3, 16, v3
	v_lshlrev_b32_e32 v32, 16, v32
	v_lshlrev_b32_e32 v33, 16, v33
	v_pk_add_f32 v[6:7], v[6:7], v[10:11] neg_lo:[0,1] neg_hi:[0,1]
	v_cvt_pk_bf16_f32 v10, v10, v11
	v_cvt_pk_bf16_f32 v11, v2, v3
	v_cvt_pk_bf16_f32 v12, v12, v13
	v_cvt_pk_bf16_f32 v13, v32, v33
	v_pk_add_f32 v[18:19], v[48:49], v[14:15] neg_lo:[0,1] neg_hi:[0,1]
	v_pk_add_f32 v[20:21], v[46:47], v[16:17] neg_lo:[0,1] neg_hi:[0,1]
	v_cvt_pk_bf16_f32 v14, v14, v15
	v_cvt_pk_bf16_f32 v15, v16, v17
	v_cvt_pk_bf16_f32 v16, v22, v23
	v_cvt_pk_bf16_f32 v17, v26, v27
	v_pk_add_f32 v[24:25], v[44:45], v[22:23] neg_lo:[0,1] neg_hi:[0,1]
	v_pk_add_f32 v[28:29], v[42:43], v[26:27] neg_lo:[0,1] neg_hi:[0,1]
	v_mfma_f32_32x32x16_bf16 a[0:15], v[10:13], v[14:17], a[0:15]
	v_add_f32_e64 v8, v8, -v2
	v_add_f32_e64 v9, v9, -v3
	v_add_f32_e64 v22, v4, -v32
	v_add_f32_e64 v23, v5, -v33
	v_cvt_pk_bf16_f32 v2, v18, v19
	v_cvt_pk_bf16_f32 v3, v20, v21
	v_cvt_pk_bf16_f32 v4, v24, v25
	v_cvt_pk_bf16_f32 v5, v28, v29
	v_cvt_pk_bf16_f32 v6, v6, v7
	v_cvt_pk_bf16_f32 v7, v8, v9
	v_mfma_f32_32x32x16_bf16 a[0:15], v[10:13], v[2:5], a[0:15]
	v_cvt_pk_bf16_f32 v8, v30, v31
	v_cvt_pk_bf16_f32 v9, v22, v23
	v_lshrrev_b32_e32 v38, 6, v0
	s_lshl_b32 s2, s12, 2
	s_add_i32 s2, s2, 0xfffff800
	v_add_u32_e32 v38, s2, v38
	v_lshlrev_b32_e32 v38, 12, v38
	v_lshl_add_u32 v38, v1, 4, v38
	s_waitcnt lgkmcnt(0)
	v_mfma_f32_32x32x16_bf16 a[0:15], v[6:9], v[14:17], a[0:15]
	s_mov_b64 s[2:3], 0
	s_nop 7
	s_nop 4
	global_store_dwordx4 v38, a[0:3], s[14:15] sc1
	global_store_dwordx4 v38, a[4:7], s[14:15] offset:1024 sc1
	global_store_dwordx4 v38, a[8:11], s[14:15] offset:2048 sc1
	global_store_dwordx4 v38, a[12:15], s[14:15] offset:3072 sc1

.LBB1_11:
	s_lshl_b32 s0, s30, 5
	s_lshl_b32 s1, s31, 7
	s_and_b32 s13, s2, 3
	s_or_b32 s14, s0, s1
	s_lshl_b32 s4, s28, 7
	s_lshl_b32 s5, s31, 2
	s_add_i32 s4, s4, s5
	s_add_i32 s4, s4, s30
	s_lshl_b32 s4, s4, 1
	s_add_i32 s4, s4, s3
	s_lshl_b32 s4, s4, 12
	s_add_u32 s4, s18, s4
	s_addc_u32 s5, s19, 0
	v_lshlrev_b32_e32 v0, 2, v173
	s_lshl_b32 s0, s3, 5
	s_lshl_b32 s12, s13, 6
	s_mov_b32 s1, 0
	s_mov_b32 s15, 0
	global_load_dwordx4 v[124:127], v0, s[4:5]
	global_load_dwordx4 v[128:131], v0, s[4:5] offset:1024
	global_load_dwordx4 v[132:135], v0, s[4:5] offset:2048
	global_load_dwordx4 v[136:139], v0, s[4:5] offset:3072
	s_lshl_b64 s[2:3], s[14:15], 2
	v_mov_b32_e32 v37, 0
	v_lshlrev_b32_e32 v36, 2, v172
	v_lshlrev_b32_e32 v122, 16, v175
	v_mov_b32_e32 v123, 0
	s_mul_i32 s4, s29, 0x2200
	s_add_i32 s4, s4, 0
	v_mov_b32_e32 v8, v141
	v_add_u32_e32 v9, s4, v173
	s_xor_b32 s4, s29, 4
	v_permlane32_swap_b32_e32 v141, v8
	s_mulk_i32 s4, 0x2200
	v_add_f32_e32 v8, v141, v8
	s_add_i32 s4, s4, 0
	ds_write2st64_b32 v9, v146, v8 offset1:1
	ds_write2st64_b32 v9, v54, v55 offset0:2 offset1:3
	ds_write2st64_b32 v9, v38, v39 offset0:18 offset1:19
	ds_write2st64_b32 v9, v56, v57 offset0:4 offset1:5
	ds_write2st64_b32 v9, v40, v41 offset0:20 offset1:21
	ds_write2st64_b32 v9, v58, v59 offset0:6 offset1:7
	ds_write2st64_b32 v9, v42, v43 offset0:22 offset1:23
	ds_write2st64_b32 v9, v60, v61 offset0:8 offset1:9
	ds_write2st64_b32 v9, v44, v45 offset0:24 offset1:25
	ds_write2st64_b32 v9, v62, v63 offset0:10 offset1:11
	ds_write2st64_b32 v9, v46, v47 offset0:26 offset1:27
	ds_write2st64_b32 v9, v64, v65 offset0:12 offset1:13
	ds_write2st64_b32 v9, v48, v49 offset0:28 offset1:29
	ds_write2st64_b32 v9, v66, v67 offset0:14 offset1:15
	ds_write2st64_b32 v9, v50, v51 offset0:30 offset1:31
	ds_write2st64_b32 v9, v68, v69 offset0:16 offset1:17
	ds_write2st64_b32 v9, v52, v53 offset0:32 offset1:33
	v_add_u32_e32 v66, s4, v173
	s_waitcnt lgkmcnt(0)
	s_barrier
	ds_read2st64_b32 v[10:11], v66 offset1:1
	ds_read2st64_b32 v[12:13], v66 offset0:2 offset1:3
	ds_read2st64_b32 v[14:15], v66 offset0:4 offset1:5
	ds_read2st64_b32 v[38:39], v66 offset0:6 offset1:7
	v_max_f32_e32 v40, v146, v146
	s_waitcnt lgkmcnt(3)
	v_max_f32_e32 v9, v10, v10
	v_max_f32_e32 v9, v40, v9
	v_sub_f32_e32 v40, v146, v9
	v_sub_f32_e32 v9, v10, v9
	v_exp_f32_e32 v40, v40
	v_exp_f32_e32 v41, v9
	v_mov_b32_e32 v9, v11
	v_pk_mul_f32 v[8:9], v[8:9], v[40:41]
	s_nop 0
	v_add_f32_e32 v8, v8, v9
	v_div_scale_f32 v9, s[4:5], v8, v8, 1.0
	v_rcp_f32_e32 v10, v9
	s_nop 0
	v_fma_f32 v11, -v9, v10, 1.0
	v_fmac_f32_e32 v10, v11, v10
	v_div_scale_f32 v11, vcc, 1.0, v8, 1.0
	v_mul_f32_e32 v42, v11, v10
	v_fma_f32 v43, -v9, v42, v11
	v_fmac_f32_e32 v42, v43, v10
	v_fma_f32 v9, -v9, v42, v11
	v_div_fmas_f32 v9, v9, v10, v42
	v_div_fixup_f32 v9, v9, v8, 1.0
	v_mul_f32_e32 v8, v40, v9
	v_mul_f32_e32 v10, v41, v9
	ds_read2st64_b32 v[40:41], v66 offset0:18 offset1:19
	ds_read2st64_b32 v[42:43], v66 offset0:20 offset1:21
	ds_read2st64_b32 v[44:45], v66 offset0:22 offset1:23
	ds_read2st64_b32 v[46:47], v66 offset0:16 offset1:17
	s_waitcnt lgkmcnt(6)
	v_pk_mul_f32 v[12:13], v[10:11], v[12:13] op_sel_hi:[0,1]
	s_waitcnt lgkmcnt(5)
	v_pk_mul_f32 v[14:15], v[10:11], v[14:15] op_sel_hi:[0,1]
	s_waitcnt lgkmcnt(4)
	v_pk_mul_f32 v[38:39], v[10:11], v[38:39] op_sel_hi:[0,1]
	s_waitcnt lgkmcnt(3)
	v_pk_mul_f32 v[40:41], v[10:11], v[40:41] op_sel_hi:[0,1]
	v_pk_fma_f32 v[48:49], v[8:9], v[70:71], v[40:41] op_sel_hi:[0,1,1]
	s_waitcnt lgkmcnt(2)
	v_pk_mul_f32 v[40:41], v[10:11], v[42:43] op_sel_hi:[0,1]
	v_pk_fma_f32 v[50:51], v[8:9], v[72:73], v[40:41] op_sel_hi:[0,1,1]
	s_waitcnt lgkmcnt(1)
	v_pk_mul_f32 v[40:41], v[10:11], v[44:45] op_sel_hi:[0,1]
	v_pk_fma_f32 v[52:53], v[8:9], v[74:75], v[40:41] op_sel_hi:[0,1,1]
	ds_read2st64_b32 v[40:41], v66 offset0:8 offset1:9
	ds_read2st64_b32 v[42:43], v66 offset0:24 offset1:25
	ds_read2st64_b32 v[44:45], v66 offset0:10 offset1:11
	ds_read2st64_b32 v[54:55], v66 offset0:12 offset1:13
	ds_read2st64_b32 v[56:57], v66 offset0:14 offset1:15
	ds_read2st64_b32 v[58:59], v66 offset0:26 offset1:27
	ds_read2st64_b32 v[60:61], v66 offset0:28 offset1:29
	ds_read2st64_b32 v[62:63], v66 offset0:30 offset1:31
	s_waitcnt lgkmcnt(6)
	v_pk_mul_f32 v[42:43], v[10:11], v[42:43] op_sel_hi:[0,1]
	v_pk_fma_f32 v[64:65], v[8:9], v[76:77], v[42:43] op_sel_hi:[0,1,1]
	s_waitcnt lgkmcnt(5)
	v_pk_mul_f32 v[42:43], v[10:11], v[44:45] op_sel_hi:[0,1]
	s_waitcnt lgkmcnt(2)
	v_pk_mul_f32 v[44:45], v[10:11], v[58:59] op_sel_hi:[0,1]
	v_pk_fma_f32 v[58:59], v[8:9], v[78:79], v[44:45] op_sel_hi:[0,1,1]
	v_pk_mul_f32 v[44:45], v[10:11], v[54:55] op_sel_hi:[0,1]
	s_waitcnt lgkmcnt(1)
	v_pk_mul_f32 v[54:55], v[10:11], v[60:61] op_sel_hi:[0,1]
	ds_read2st64_b32 v[60:61], v66 offset0:32 offset1:33
	s_waitcnt vmcnt(0)
	v_pk_mul_f32 v[40:41], v[10:11], v[40:41] op_sel_hi:[0,1]
	v_cvt_pk_bf16_f32 v0, v208, v209
	v_cvt_pk_bf16_f32 v1, v210, v211
	v_cvt_pk_bf16_f32 v2, v212, v213
	v_cvt_pk_bf16_f32 v3, v214, v215
	v_pk_fma_f32 v[12:13], v[8:9], v[86:87], v[12:13] op_sel_hi:[0,1,1]
	v_pk_fma_f32 v[14:15], v[8:9], v[88:89], v[14:15] op_sel_hi:[0,1,1]
	v_pk_fma_f32 v[38:39], v[8:9], v[90:91], v[38:39] op_sel_hi:[0,1,1]
	v_pk_fma_f32 v[40:41], v[8:9], v[92:93], v[40:41] op_sel_hi:[0,1,1]
	v_pk_mul_f32 v[56:57], v[10:11], v[56:57] op_sel_hi:[0,1]
	s_waitcnt lgkmcnt(1)
	v_pk_mul_f32 v[62:63], v[10:11], v[62:63] op_sel_hi:[0,1]
	v_pk_mul_f32 v[46:47], v[10:11], v[46:47] op_sel_hi:[0,1]
	s_waitcnt lgkmcnt(0)
	v_pk_mul_f32 v[10:11], v[10:11], v[60:61] op_sel_hi:[0,1]
	v_cvt_pk_bf16_f32 v4, v12, v13
	v_cvt_pk_bf16_f32 v5, v14, v15
	v_cvt_pk_bf16_f32 v6, v38, v39
	v_cvt_pk_bf16_f32 v7, v40, v41
	v_pk_fma_f32 v[42:43], v[8:9], v[94:95], v[42:43] op_sel_hi:[0,1,1]
	v_pk_fma_f32 v[44:45], v[8:9], v[96:97], v[44:45] op_sel_hi:[0,1,1]
	v_pk_fma_f32 v[54:55], v[8:9], v[80:81], v[54:55] op_sel_hi:[0,1,1]
	v_pk_fma_f32 v[56:57], v[8:9], v[98:99], v[56:57] op_sel_hi:[0,1,1]
	v_pk_fma_f32 v[62:63], v[8:9], v[82:83], v[62:63] op_sel_hi:[0,1,1]
	v_pk_fma_f32 v[46:47], v[8:9], v[100:101], v[46:47] op_sel_hi:[0,1,1]
	v_pk_fma_f32 v[60:61], v[8:9], v[84:85], v[10:11] op_sel_hi:[0,1,1]
	v_mfma_f32_32x32x16_bf16 v[0:15], v[0:3], v[4:7], 0
	v_cvt_pk_bf16_f32 v42, v42, v43
	v_cvt_pk_bf16_f32 v38, v216, v217
	v_cvt_pk_bf16_f32 v39, v218, v219
	v_cvt_pk_bf16_f32 v40, v220, v221
	v_cvt_pk_bf16_f32 v41, v222, v223
	v_cvt_pk_bf16_f32 v43, v44, v45
	v_cvt_pk_bf16_f32 v44, v56, v57
	v_cvt_pk_bf16_f32 v45, v46, v47
	s_nop 1
	v_mfma_f32_32x32x16_bf16 v[0:15], v[38:41], v[42:45], v[0:15]
	v_cvt_pk_bf16_f32 v38, v224, v225
	v_cvt_pk_bf16_f32 v39, v226, v227
	v_cvt_pk_bf16_f32 v40, v228, v229
	v_cvt_pk_bf16_f32 v41, v230, v231
	v_cvt_pk_bf16_f32 v42, v48, v49
	v_cvt_pk_bf16_f32 v43, v50, v51
	v_cvt_pk_bf16_f32 v44, v52, v53
	v_cvt_pk_bf16_f32 v45, v64, v65
	v_cvt_pk_bf16_f32 v32, v232, v233
	v_cvt_pk_bf16_f32 v33, v234, v235
	v_mfma_f32_32x32x16_bf16 v[0:15], v[38:41], v[42:45], v[0:15]
	v_cvt_pk_bf16_f32 v34, v236, v237
	v_cvt_pk_bf16_f32 v35, v238, v239
	v_cvt_pk_bf16_f32 v38, v58, v59
	v_add_f32_e32 v42, 1.0, v205
	v_div_scale_f32 v43, s[4:5], v42, v42, 1.0
	v_rcp_f32_e32 v44, v43
	v_cvt_pk_bf16_f32 v39, v54, v55
	v_cvt_pk_bf16_f32 v40, v62, v63
	v_cvt_pk_bf16_f32 v41, v60, v61
	s_lshl_b32 s4, s28, 8
	s_or_b32 s4, s4, s12
	v_mfma_f32_32x32x16_bf16 v[0:15], v[32:35], v[38:41], v[0:15]
	v_fma_f32 v32, -v43, v44, 1.0
	v_fmac_f32_e32 v44, v32, v44
	v_div_scale_f32 v32, vcc, 1.0, v42, 1.0
	s_add_i32 s0, s4, s0
	v_mul_f32_e32 v33, v32, v44
	s_lshl_b64 s[0:1], s[0:1], 14
	v_fma_f32 v34, -v43, v33, v32
	s_add_u32 s0, s10, s0
	v_fmac_f32_e32 v33, v34, v44
	s_addc_u32 s1, s11, s1
	v_fma_f32 v32, -v43, v33, v32
	s_add_u32 s0, s0, s2
	v_div_fmas_f32 v32, v32, v44, v33
	s_addc_u32 s1, s1, s3
	v_add_f32_e32 v0, v0, v240
	v_div_fixup_f32 v34, v32, v42, 1.0
	v_lshl_add_u64 v[32:33], s[0:1], 0, v[36:37]
	v_fmac_f32_e32 v124, v205, v0
	v_mul_f32_e32 v0, v34, v124
	v_lshl_add_u64 v[32:33], v[32:33], 0, v[122:123]
	global_store_dword v[32:33], v0, off sc1
	v_add_f32_e32 v0, v1, v241
	s_movk_i32 s0, 0x4000
	v_fmac_f32_e32 v125, v205, v0
	v_add_co_u32_e32 v0, vcc, s0, v32
	v_mul_f32_e32 v28, v34, v125
	s_nop 0
	v_addc_co_u32_e32 v1, vcc, 0, v33, vcc
	global_store_dword v[0:1], v28, off sc1
	v_add_f32_e32 v0, v2, v242
	s_mov_b32 s0, 0x8000
	v_fmac_f32_e32 v126, v205, v0
	v_add_co_u32_e32 v0, vcc, s0, v32
	v_mul_f32_e32 v2, v34, v126
	s_nop 0
	v_addc_co_u32_e32 v1, vcc, 0, v33, vcc
	global_store_dword v[0:1], v2, off sc1
	v_add_f32_e32 v0, v3, v243
	s_mov_b32 s0, 0xc000
	v_fmac_f32_e32 v127, v205, v0
	v_add_co_u32_e32 v0, vcc, s0, v32
	v_mul_f32_e32 v2, v34, v127
	s_nop 0
	v_addc_co_u32_e32 v1, vcc, 0, v33, vcc
	global_store_dword v[0:1], v2, off sc1
	v_add_f32_e32 v0, v4, v244
	s_mov_b32 s0, 0x20000
	v_fmac_f32_e32 v128, v205, v0
	v_add_co_u32_e32 v0, vcc, s0, v32
	v_mul_f32_e32 v2, v34, v128
	s_nop 0
	v_addc_co_u32_e32 v1, vcc, 0, v33, vcc
	global_store_dword v[0:1], v2, off sc1
	v_add_f32_e32 v0, v5, v245
	s_mov_b32 s0, 0x24000
	v_fmac_f32_e32 v129, v205, v0
	v_add_co_u32_e32 v0, vcc, s0, v32
	v_mul_f32_e32 v2, v34, v129
	s_nop 0
	v_addc_co_u32_e32 v1, vcc, 0, v33, vcc
	global_store_dword v[0:1], v2, off sc1
	v_add_f32_e32 v0, v6, v246
	s_mov_b32 s0, 0x28000
	v_fmac_f32_e32 v130, v205, v0
	v_add_co_u32_e32 v0, vcc, s0, v32
	v_mul_f32_e32 v2, v34, v130
	s_nop 0
	v_addc_co_u32_e32 v1, vcc, 0, v33, vcc
	global_store_dword v[0:1], v2, off sc1
	v_add_f32_e32 v0, v7, v247
	s_mov_b32 s0, 0x2c000
	v_fmac_f32_e32 v131, v205, v0
	v_add_co_u32_e32 v0, vcc, s0, v32
	v_mul_f32_e32 v2, v34, v131
	s_nop 0
	v_addc_co_u32_e32 v1, vcc, 0, v33, vcc
	global_store_dword v[0:1], v2, off sc1
	v_add_f32_e32 v0, v8, v248
	s_mov_b32 s0, 0x40000
	v_fmac_f32_e32 v132, v205, v0
	v_add_co_u32_e32 v0, vcc, s0, v32
	v_mul_f32_e32 v2, v34, v132
	s_nop 0
	v_addc_co_u32_e32 v1, vcc, 0, v33, vcc
	global_store_dword v[0:1], v2, off sc1
	v_add_f32_e32 v0, v9, v249
	s_mov_b32 s0, 0x44000
	v_fmac_f32_e32 v133, v205, v0
	v_add_co_u32_e32 v0, vcc, s0, v32
	v_mul_f32_e32 v2, v34, v133
	s_nop 0
	v_addc_co_u32_e32 v1, vcc, 0, v33, vcc
	global_store_dword v[0:1], v2, off sc1
	v_add_f32_e32 v0, v10, v250
	s_mov_b32 s0, 0x48000
	v_fmac_f32_e32 v134, v205, v0
	v_add_co_u32_e32 v0, vcc, s0, v32
	v_mul_f32_e32 v2, v34, v134
	s_nop 0
	v_addc_co_u32_e32 v1, vcc, 0, v33, vcc
	global_store_dword v[0:1], v2, off sc1
	v_add_f32_e32 v0, v11, v251
	s_mov_b32 s0, 0x4c000
	v_fmac_f32_e32 v135, v205, v0
	v_add_co_u32_e32 v0, vcc, s0, v32
	v_mul_f32_e32 v2, v34, v135
	s_nop 0
	v_addc_co_u32_e32 v1, vcc, 0, v33, vcc
	global_store_dword v[0:1], v2, off sc1
	v_add_f32_e32 v0, v12, v252
	s_mov_b32 s0, 0x60000
	v_fmac_f32_e32 v136, v205, v0
	v_add_co_u32_e32 v0, vcc, s0, v32
	v_mul_f32_e32 v2, v34, v136
	s_nop 0
	v_addc_co_u32_e32 v1, vcc, 0, v33, vcc
	global_store_dword v[0:1], v2, off sc1
	v_add_f32_e32 v0, v13, v253
	s_mov_b32 s0, 0x64000
	v_fmac_f32_e32 v137, v205, v0
	v_add_co_u32_e32 v0, vcc, s0, v32
	v_mul_f32_e32 v2, v34, v137
	s_nop 0
	v_addc_co_u32_e32 v1, vcc, 0, v33, vcc
	global_store_dword v[0:1], v2, off sc1
	v_add_f32_e32 v0, v14, v254
	s_mov_b32 s0, 0x68000
	v_fmac_f32_e32 v138, v205, v0
	v_add_co_u32_e32 v0, vcc, s0, v32
	v_mul_f32_e32 v2, v34, v138
	s_nop 0
	v_addc_co_u32_e32 v1, vcc, 0, v33, vcc
	global_store_dword v[0:1], v2, off sc1
	v_add_f32_e32 v0, v15, v255
	v_fmac_f32_e32 v139, v205, v0
	v_add_co_u32_e32 v0, vcc, 0x6c000, v32
	v_mul_f32_e32 v2, v34, v139
	s_nop 0
	v_addc_co_u32_e32 v1, vcc, 0, v33, vcc
	global_store_dword v[0:1], v2, off sc1
	s_endpgm
